# row-tile hand-offs now use per-member flag words written with plain stores and polled with sc1 loads inside the XCD's L2 (no fabric atomics)
# speedup vs baseline: 1.0102x; 1.0005x over previous
; __device__ __forceinline__ unsigned xb_ld(unsigned* p)              { return __hip_atomic_load(p, __ATOMIC_RELAXED, __HIP_MEMORY_SCOPE_AGENT); }
; __device__ __forceinline__ unsigned xb_add(unsigned* p, unsigned v) { return __hip_atomic_fetch_add(p, v, __ATOMIC_RELAXED, __HIP_MEMORY_SCOPE_AGENT); }
; #define XB_SPIN(cond, bar) do { unsigned _sp = 0; while (cond) { __builtin_amdgcn_s_sleep(1); \
;     if ((++_sp & 255u) == 0u) { if (xb_ld(&(bar)[XB_TMO])) break; if (_sp > XB_SPIN_CAP) { atomicAdd(&(bar)[XB_TMO], 1u); break; } } } } while (0)
; __device__ __forceinline__ void xcd_barrier(const XcdBarrier& b) {
;   asm volatile("s_waitcnt vmcnt(0)" ::: "memory");
;   __syncthreads();
;   if (threadIdx.x == 0) {
;     unsigned* bar = b.bar;
;     __builtin_amdgcn_s_waitcnt(0);
;     unsigned nloc = b.st[0], nx = b.st[1];
;     if (nloc == 0u) { xcd_barrier_complete(bar, b.x, nloc, nx); b.st[0] = nloc; b.st[1] = nx; }
;     const unsigned old = xb_add(&bar[XB_XSUB(b.x)], 1u);
;     const unsigned gen = old / nloc;
;     if (old + 1u == (gen + 1u) * nloc) {
;       __builtin_amdgcn_fence(__ATOMIC_RELEASE, "agent");
;       asm volatile("s_waitcnt vmcnt(0)" ::: "memory");
;       const unsigned og = xb_add(&bar[XB_TOP], 1u);
;       const unsigned tg = og / nx;
;       if (og + 1u == (tg + 1u) * nx) xb_add(&bar[XB_TOPGEN], 1u);
;       else XB_SPIN(xb_ld(&bar[XB_TOPGEN]) == tg, bar);
;       __builtin_amdgcn_fence(__ATOMIC_ACQUIRE, "agent");
;       xb_add(&bar[XB_XGEN(b.x)], 1u);
;       asm volatile("s_waitcnt vmcnt(0)" ::: "memory");
;     } else {
;       XB_SPIN(xb_ld(&bar[XB_XGEN(b.x)]) == gen, bar);
;       __builtin_amdgcn_fence(__ATOMIC_ACQUIRE, "agent");
;       asm volatile("s_waitcnt vmcnt(0)" ::: "memory");
;     }
;   }
;   __syncthreads();
; }
.LBB0_1072:
	s_waitcnt vmcnt(0)
	s_waitcnt vmcnt(63) expcnt(7) lgkmcnt(15)
	s_barrier
	s_and_saveexec_b64 s[12:13], s[4:5]
	s_cbranch_execz .LBB0_1124
	s_waitcnt vmcnt(0) lgkmcnt(0)
	v_mov_b32_e32 v253, 0x12818
	ds_read_b32 v254, v253 offset:4
	ds_read_b32 v253, v253
	s_waitcnt lgkmcnt(0)
	v_cmp_ne_u32_e32 vcc, 0, v254
	s_cbranch_vccnz .Lmy_gbar_8
	v_readfirstlane_b32 s99, v253
	s_nop 0
	s_and_b32 s100, s99, 7
	s_bfe_u32 s101, s99, 0x30003
	s_lshl_b32 s100, s100, 3
	s_or_b32 s100, s100, s101
	s_lshr_b32 s101, s100, 2
	s_add_u32 s101, s101, 28
	s_lshl_b32 s101, s101, 8
	s_and_b32 s100, s100, 3
	s_lshl_b32 s100, s100, 5
	s_add_u32 s101, s101, s100
	s_lshr_b32 s100, s99, 6
	s_mov_b64 exec, 0xff
	v_mbcnt_lo_u32_b32 v254, -1, 0
	v_lshl_add_u32 v253, v254, 2, s101
	v_cmp_eq_u32_e32 vcc, s100, v254
	v_mov_b32_e32 v254, 1
	s_and_b64 exec, exec, vcc
	global_store_dword v253, v254, s[44:45] offset:128
	s_mov_b64 exec, 0xff
	buffer_inv sc1
	s_mov_b32 s100, 0
.Lmy_gs_w_8:
	global_load_dword v254, v253, s[44:45] offset:128 sc1
	s_waitcnt vmcnt(0)
	v_cmp_le_u32_e32 vcc, 1, v254
	s_cmpk_eq_u32 vcc_lo, 0xff
	s_cbranch_scc1 .Lmy_gs_d_8
	s_sleep 1
	s_add_u32 s100, s100, 1
	s_cmp_lt_u32 s100, 0x1000
	s_cbranch_scc1 .Lmy_gs_w_8
.Lmy_gs_d_8:
	s_mov_b64 exec, 1
	s_branch .Lgb_wd_8

; __device__ __forceinline__ unsigned xb_ld(unsigned* p)              { return __hip_atomic_load(p, __ATOMIC_RELAXED, __HIP_MEMORY_SCOPE_AGENT); }
; __device__ __forceinline__ unsigned xb_add(unsigned* p, unsigned v) { return __hip_atomic_fetch_add(p, v, __ATOMIC_RELAXED, __HIP_MEMORY_SCOPE_AGENT); }
; #define XB_SPIN(cond, bar) do { unsigned _sp = 0; while (cond) { __builtin_amdgcn_s_sleep(1); \
;     if ((++_sp & 255u) == 0u) { if (xb_ld(&(bar)[XB_TMO])) break; if (_sp > XB_SPIN_CAP) { atomicAdd(&(bar)[XB_TMO], 1u); break; } } } } while (0)
; __device__ __forceinline__ void xcd_barrier(const XcdBarrier& b) {
;   asm volatile("s_waitcnt vmcnt(0)" ::: "memory");
;   __syncthreads();
;   if (threadIdx.x == 0) {
;     unsigned* bar = b.bar;
;     __builtin_amdgcn_s_waitcnt(0);
;     unsigned nloc = b.st[0], nx = b.st[1];
;     if (nloc == 0u) { xcd_barrier_complete(bar, b.x, nloc, nx); b.st[0] = nloc; b.st[1] = nx; }
;     const unsigned old = xb_add(&bar[XB_XSUB(b.x)], 1u);
;     const unsigned gen = old / nloc;
;     if (old + 1u == (gen + 1u) * nloc) {
;       __builtin_amdgcn_fence(__ATOMIC_RELEASE, "agent");
;       asm volatile("s_waitcnt vmcnt(0)" ::: "memory");
;       const unsigned og = xb_add(&bar[XB_TOP], 1u);
;       const unsigned tg = og / nx;
;       if (og + 1u == (tg + 1u) * nx) xb_add(&bar[XB_TOPGEN], 1u);
;       else XB_SPIN(xb_ld(&bar[XB_TOPGEN]) == tg, bar);
;       __builtin_amdgcn_fence(__ATOMIC_ACQUIRE, "agent");
;       xb_add(&bar[XB_XGEN(b.x)], 1u);
;       asm volatile("s_waitcnt vmcnt(0)" ::: "memory");
;     } else {
;       XB_SPIN(xb_ld(&bar[XB_XGEN(b.x)]) == gen, bar);
;       __builtin_amdgcn_fence(__ATOMIC_ACQUIRE, "agent");
;       asm volatile("s_waitcnt vmcnt(0)" ::: "memory");
;     }
.LBB0_1131:
	s_or_b64 exec, exec, s[20:21]
	s_waitcnt vmcnt(0)
	s_barrier
	s_and_saveexec_b64 s[8:9], s[4:5]
	s_cbranch_execz .LBB0_1183
	s_waitcnt vmcnt(0) lgkmcnt(0)
	v_mov_b32_e32 v253, 0x12818
	ds_read_b32 v254, v253 offset:4
	ds_read_b32 v253, v253
	s_waitcnt lgkmcnt(0)
	v_cmp_ne_u32_e32 vcc, 0, v254
	s_cbranch_vccnz .Lmy_gbar_9
	v_readfirstlane_b32 s99, v253
	s_nop 0
	s_and_b32 s100, s99, 7
	s_bfe_u32 s101, s99, 0x30003
	s_lshl_b32 s100, s100, 3
	s_or_b32 s100, s100, s101
	s_lshr_b32 s101, s100, 2
	s_add_u32 s101, s101, 28
	s_lshl_b32 s101, s101, 8
	s_and_b32 s100, s100, 3
	s_lshl_b32 s100, s100, 5
	s_add_u32 s101, s101, s100
	s_lshr_b32 s100, s99, 6
	s_mov_b64 exec, 0xff
	v_mbcnt_lo_u32_b32 v254, -1, 0
	v_lshl_add_u32 v253, v254, 2, s101
	v_cmp_eq_u32_e32 vcc, s100, v254
	v_mov_b32_e32 v254, 2
	s_and_b64 exec, exec, vcc
	global_store_dword v253, v254, s[44:45] offset:128
	s_mov_b64 exec, 0xff
	buffer_inv sc1
	s_mov_b32 s100, 0
.Lmy_gs_w_9:
	global_load_dword v254, v253, s[44:45] offset:128 sc1
	s_waitcnt vmcnt(0)
	v_cmp_le_u32_e32 vcc, 2, v254
	s_cmpk_eq_u32 vcc_lo, 0xff
	s_cbranch_scc1 .Lmy_gs_d_9
	s_sleep 1
	s_add_u32 s100, s100, 1
	s_cmp_lt_u32 s100, 0x1000
	s_cbranch_scc1 .Lmy_gs_w_9
